# P8 dn-conversion stagger: five groups (entry, after units 1,3,5,7) instead of four, so slots do not overlap
# speedup vs baseline: 1.0336x; 1.0202x over previous
.LBB0_899:
	s_cmp_lt_i32 s88, 9
	s_cselect_b64 s[58:59], -1, 0
	s_and_b64 s[2:3], s[58:59], s[2:3]
	s_andn2_b64 vcc, exec, s[2:3]
	s_cbranch_vccnz .LBB0_1151
	v_readlane_b32 s2, v255, 0
	s_nop 3
	s_lshr_b32 s2, s2, 3
	s_mul_i32 s2, s2, 5
	s_lshr_b32 s2, s2, 5
	s_cmp_lg_u32 s2, 0
	s_cselect_b64 s[2:3], -1, 0
	s_mov_b32 s87, 0
	s_mov_b32 s88, 64
	v_writelane_b32 v252, s2, 12
	s_and_b64 vcc, exec, s[2:3]
	s_nop 0
	v_writelane_b32 v252, s3, 13
	s_cbranch_vccnz .LBB0_906
	v_writelane_b32 v255, 1, 5
	v_writelane_b32 v255, 64, 6
	s_branch .Lmy_cvdn

.LBB0_1107:
	s_add_u32 s66, s18, 0x210000
	s_addc_u32 s67, s19, 0
	s_add_u32 s12, s18, 0x1b800000
	v_and_b32_e32 v8, 15, v0
	s_addc_u32 s13, s19, 0
	v_lshl_or_b32 v9, s14, 6, v8
	s_lshl_b32 s3, s14, 13
	s_lshl_b32 s14, s15, 5
	s_and_b32 s16, s14, 0x60
	v_readlane_b32 s68, v255, 0
	s_nop 3
	s_lshr_b32 s68, s68, 3
	s_mul_i32 s68, s68, 5
	s_lshr_b32 s68, s68, 5
	s_lshl_b32 s68, s68, 1
	s_lshl_b32 s17, s16, 7
	s_add_i32 s68, s68, -1
	s_mov_b32 s26, s70
	s_add_i32 s70, s25, 0x18000
	s_mov_b64 s[28:29], 0x80
	s_add_i32 s72, s25, 0x1a000
	v_lshl_add_u64 v[4:5], v[4:5], 0, s[28:29]
	s_mov_b32 m0, s70
	s_add_u32 s30, s18, 0x23000080
	v_and_b32_e32 v10, 48, v0
	v_lshlrev_b32_e32 v11, 6, v0
	s_movk_i32 s14, 0x3c0
	s_waitcnt vmcnt(2)
	s_barrier
	global_load_lds_dwordx4 v[4:5], off
	v_lshl_add_u64 v[2:3], v[2:3], 0, s[28:29]
	s_mov_b32 m0, s72
	s_addc_u32 s31, s19, 0
	s_add_i32 s74, s25, 0x8000
	s_add_i32 s76, s25, 0xa000
	v_lshl_or_b32 v8, v8, 6, v10
	v_and_or_b32 v10, v11, s14, v10
	global_load_lds_dwordx4 v[2:3], off
	v_lshl_add_u64 v[2:3], s[30:31], 0, v[66:67]
	s_mov_b32 m0, s74
	s_add_u32 s14, s4, 0x40080
	global_load_lds_dwordx4 v[2:3], off
	v_lshl_add_u64 v[2:3], s[30:31], 0, v[202:203]
	s_mov_b32 m0, s76
	s_addc_u32 s15, s5, 0
	s_add_i32 s78, s25, 0x1c000
	global_load_lds_dwordx4 v[2:3], off
	v_lshl_add_u64 v[2:3], s[14:15], 0, v[198:199]
	s_mov_b32 m0, s78
	s_add_i32 s80, s25, 0x1e000
	global_load_lds_dwordx4 v[2:3], off
	v_lshl_add_u64 v[2:3], s[14:15], 0, v[200:201]
	s_mov_b32 m0, s80
	s_cmp_lt_u32 s10, 64
	global_load_lds_dwordx4 v[2:3], off
	s_cselect_b64 s[34:35], -1, 0
	s_add_i32 s14, s17, 0
	s_cmpk_lt_u32 s10, 0x100
	s_cselect_b64 s[36:37], -1, 0
	s_add_i32 s10, 0, 0x26500
	v_lshlrev_b32_e32 v11, 2, v0
	v_lshl_add_u32 v5, v6, 2, s10
	s_lshl_b32 s10, s16, 2
	v_and_b32_e32 v12, 32, v11
	s_add_u32 s85, s18, 0x4d800000
	v_xad_u32 v3, v10, v12, s14
	s_addc_u32 s86, s19, 0
	s_ashr_i32 s14, s94, 2
	v_writelane_b32 v252, s14, 19
	s_lshr_b32 s14, s14, 3
	v_add3_u32 v203, v5, v7, s10
	s_lshl_b32 s10, s26, 18
	s_lshl_b32 s15, s14, 11
	v_readlane_b32 s17, v252, 6
	s_add_i32 s91, s10, s15
	s_lshl_b32 s10, s17, 5
	s_add_i32 s91, s91, s10
	s_lshr_b32 s10, s92, 2
	s_lshl_b32 s27, s26, 13
	s_lshl_b32 s15, s10, 8
	s_and_b32 s38, s94, 7
	v_or_b32_e32 v238, s16, v6
	v_writelane_b32 v252, s15, 7
	s_lshl_b32 s94, s10, 9
	s_lshl_b32 s16, s14, 7
	s_lshl_b32 s97, s10, 4
	s_lshl_b32 s82, s10, 5
	s_lshl_b32 s81, s10, 3
	s_add_i32 s10, s17, s27
	s_lshl_b32 s14, s14, 6
	v_lshrrev_b32_e32 v5, 1, v0
	v_writelane_b32 v252, s27, 20
	s_add_i32 s10, s10, s14
	s_lshl_b32 s14, s38, 3
	s_waitcnt vmcnt(6)
	v_and_b32_e32 v5, 16, v5
	s_lshl_b32 s15, s26, 14
	v_writelane_b32 v252, s38, 21
	s_add_i32 s10, s10, s14
	v_xad_u32 v4, v8, v12, 0
	v_and_b32_e32 v2, 0xfc, v11
	v_or_b32_e32 v7, 32, v5
	v_add_u32_e32 v8, 0x80, v9
	s_bfe_u32 s40, s92, 0x1d0002
	s_add_i32 s96, s15, s16
	s_lshl_b32 s15, s17, 1
	v_writelane_b32 v252, s10, 9
	s_mov_b32 s69, 0x18000
	s_mov_b32 s71, 0x1a000
	s_mov_b32 s73, 0x8000
	s_mov_b32 s75, 0xa000
	s_mov_b32 s77, 0x1c000
	s_mov_b32 s79, 0x1e000
	v_or_b32_e32 v218, v9, v5
	v_or_b32_e32 v219, v9, v7
	v_or_b32_e32 v220, v8, v5
	v_or_b32_e32 v221, v8, v7
	v_add_u32_e32 v222, 0x10000, v3
	v_add_u32_e32 v223, 0x10400, v3
	v_add_u32_e32 v224, 0x10800, v3
	v_add_u32_e32 v225, 0x10c00, v3
	v_add_u32_e32 v226, 0x14000, v3
	v_add_u32_e32 v227, 0x14400, v3
	v_add_u32_e32 v228, 0x14800, v3
	v_add_u32_e32 v229, 0x14c00, v3
	v_add_u32_e32 v230, 0x18000, v3
	v_add_u32_e32 v231, 0x18400, v3
	v_add_u32_e32 v232, 0x18800, v3
	v_add_u32_e32 v233, 0x18c00, v3
	v_add_u32_e32 v234, 0x1c000, v3
	v_add_u32_e32 v235, 0x1c400, v3
	v_add_u32_e32 v236, 0x1c800, v3
	v_add_u32_e32 v237, 0x1cc00, v3
	s_add_i32 s21, s27, 0x2000
	s_add_i32 s89, s20, -1
	s_lshl_b32 s90, s38, 8
	s_lshl_b32 s95, s38, 4
	s_add_i32 s96, s96, s15
	v_writelane_b32 v252, s40, 16
	s_lshl_b32 s10, s40, 1
	v_lshlrev_b32_e32 v239, 2, v2
	s_mov_b32 s15, 0xc000
	s_mov_b32 s84, 0xe000
	v_mov_b32_e32 v240, 0x7f7f7f7f
	s_mov_b32 s38, 0x3c800000
	s_mov_b32 s93, 0xc0e00000
	s_movk_i32 s14, 0x1000
	v_add_u32_e32 v241, s3, v4
	v_mov_b32_e32 v242, 0x40e00000
	v_mov_b32_e32 v247, v66
	s_mov_b32 s92, 0
	s_barrier
	v_writelane_b32 v252, s10, 10
